# prep kernel stores made write-through (sc0 sc1) so the kernel boundary has no dirty L2 lines to write back
# baseline (speedup 1.0000x reference)
.LBB0_4:
	s_load_dwordx2 s[6:7], s[0:1], 0x58
	v_lshlrev_b32_e32 v2, 6, v0
	v_mov_b32_e32 v3, 0
	s_waitcnt lgkmcnt(0)
	v_lshl_add_u64 v[4:5], v[2:3], 2, s[6:7]
	global_store_dword v[4:5], v3, off sc0 sc1
	s_or_b64 exec, exec, s[4:5]
	s_cmpk_gt_i32 s2, 0xff
	s_mov_b64 s[4:5], -1
	s_cbranch_scc0 .LBB0_2
.LBB0_5:
	s_cmpk_gt_u32 s2, 0x14f
	v_lshrrev_b32_e32 v1, 7, v0
	s_cbranch_scc0 .LBB0_11
	s_load_dwordx4 s[8:11], s[0:1], 0x30
	s_lshl_b32 s3, s2, 7
	s_add_i32 s4, s3, 0xffff5800
	s_mov_b32 s5, 0
	s_lshl_b64 s[6:7], s[4:5], 2
	s_waitcnt lgkmcnt(0)
	s_add_u32 s6, s8, s6
	v_lshlrev_b32_e32 v6, 6, v1
	v_mov_b32_e32 v7, 0
	v_and_b32_e32 v4, 0x7f, v0
	s_addc_u32 s7, s9, s7
	v_lshlrev_b64 v[2:3], 9, v[6:7]
	v_lshl_add_u64 v[8:9], v[6:7], 2, s[6:7]
	v_lshl_add_u64 v[2:3], s[10:11], 0, v[2:3]
	v_lshlrev_b32_e32 v6, 2, v4
	v_lshl_add_u64 v[10:11], v[2:3], 0, v[6:7]
	global_load_dwordx4 v[12:15], v[8:9], off
	global_load_dword v7, v[10:11], off
	global_load_dword v44, v[10:11], off offset:512
	global_load_dword v45, v[10:11], off offset:1024
	global_load_dword v46, v[10:11], off offset:1536
	global_load_dwordx4 v[16:19], v[8:9], off offset:16
	global_load_dwordx4 v[2:5], v[8:9], off offset:32
	global_load_dword v47, v[10:11], off offset:2048
	global_load_dword v48, v[10:11], off offset:2560
	global_load_dword v49, v[10:11], off offset:3072
	global_load_dword v50, v[10:11], off offset:3584
	s_movk_i32 s3, 0x1000
	v_add_co_u32_e32 v24, vcc, s3, v10
	s_movk_i32 s3, 0x2000
	s_nop 0
	v_addc_co_u32_e32 v25, vcc, 0, v11, vcc
	v_add_co_u32_e32 v36, vcc, s3, v10
	s_movk_i32 s3, 0x3000
	s_nop 0
	v_addc_co_u32_e32 v37, vcc, 0, v11, vcc
	global_load_dword v51, v[36:37], off offset:-4096
	global_load_dword v52, v[24:25], off offset:512
	global_load_dword v53, v[24:25], off offset:1024
	global_load_dword v54, v[24:25], off offset:1536
	global_load_dwordx4 v[20:23], v[8:9], off offset:48
	global_load_dword v55, v[24:25], off offset:2048
	global_load_dword v56, v[24:25], off offset:2560
	global_load_dword v57, v[24:25], off offset:3072
	global_load_dword v58, v[24:25], off offset:3584
	s_nop 0
	global_load_dwordx4 v[24:27], v[8:9], off offset:96
	global_load_dwordx4 v[28:31], v[8:9], off offset:80
	global_load_dwordx4 v[32:35], v[8:9], off offset:64
	v_add_co_u32_e32 v38, vcc, s3, v10
	s_movk_i32 s5, 0x4000
	s_nop 0
	v_addc_co_u32_e32 v39, vcc, 0, v11, vcc
	v_add_co_u32_e32 v40, vcc, s5, v10
	s_movk_i32 s6, 0x7000
	s_nop 0
	v_addc_co_u32_e32 v41, vcc, 0, v11, vcc
	v_add_co_u32_e32 v42, vcc, s6, v10
	s_movk_i32 s3, 0x5000
	s_nop 0
	v_addc_co_u32_e32 v43, vcc, 0, v11, vcc
	s_waitcnt vmcnt(21)
	v_fma_f32 v7, v12, v7, 0
	s_waitcnt vmcnt(20)
	v_fmac_f32_e32 v7, v13, v44
	s_waitcnt vmcnt(19)
	v_fmac_f32_e32 v7, v14, v45
	global_load_dword v44, v[36:37], off
	global_load_dword v45, v[36:37], off offset:512
	s_waitcnt vmcnt(20)
	v_fmac_f32_e32 v7, v15, v46
	global_load_dword v46, v[36:37], off offset:1024
	global_load_dword v59, v[36:37], off offset:1536
	global_load_dword v60, v[36:37], off offset:2048
	global_load_dword v61, v[36:37], off offset:2560
	global_load_dword v62, v[36:37], off offset:3072
	global_load_dword v63, v[36:37], off offset:3584
	global_load_dword v64, v[40:41], off offset:-4096
	s_waitcnt vmcnt(24)
	v_fmac_f32_e32 v7, v16, v47
	global_load_dword v36, v[38:39], off offset:512
	s_waitcnt vmcnt(24)
	v_fmac_f32_e32 v7, v17, v48
	s_waitcnt vmcnt(23)
	v_fmac_f32_e32 v7, v18, v49
	s_waitcnt vmcnt(22)
	v_fmac_f32_e32 v7, v19, v50
	global_load_dword v37, v[38:39], off offset:1024
	global_load_dword v47, v[38:39], off offset:1536
	global_load_dword v48, v[38:39], off offset:2048
	global_load_dword v49, v[38:39], off offset:2560
	global_load_dword v50, v[38:39], off offset:3072
	global_load_dword v65, v[38:39], off offset:3584
	global_load_dword v66, v[42:43], off offset:3584
	global_load_dwordx4 v[12:15], v[8:9], off offset:112
	s_waitcnt vmcnt(29)
	v_fmac_f32_e32 v7, v2, v51
	s_waitcnt vmcnt(28)
	v_fmac_f32_e32 v7, v3, v52
	s_waitcnt vmcnt(27)
	v_fmac_f32_e32 v7, v4, v53
	s_waitcnt vmcnt(26)
	v_fmac_f32_e32 v7, v5, v54
	global_load_dwordx4 v[2:5], v[8:9], off offset:128
	global_load_dword v38, v[40:41], off
	global_load_dword v39, v[40:41], off offset:512
	global_load_dword v51, v[40:41], off offset:1024
	global_load_dword v52, v[40:41], off offset:1536
	s_waitcnt vmcnt(29)
	v_fmac_f32_e32 v7, v20, v55
	s_waitcnt vmcnt(28)
	v_fmac_f32_e32 v7, v21, v56
	s_waitcnt vmcnt(27)
	v_fmac_f32_e32 v7, v22, v57
	s_waitcnt vmcnt(26)
	v_fmac_f32_e32 v7, v23, v58
	global_load_dwordx4 v[16:19], v[8:9], off offset:144
	global_load_dword v53, v[40:41], off offset:2048
	s_waitcnt vmcnt(24)
	v_fmac_f32_e32 v7, v32, v44
	s_waitcnt vmcnt(23)
	v_fmac_f32_e32 v7, v33, v45
	s_waitcnt vmcnt(22)
	v_fmac_f32_e32 v7, v34, v46
	s_waitcnt vmcnt(21)
	v_fmac_f32_e32 v7, v35, v59
	s_waitcnt vmcnt(20)
	v_fmac_f32_e32 v7, v28, v60
	s_waitcnt vmcnt(19)
	v_fmac_f32_e32 v7, v29, v61
	s_waitcnt vmcnt(18)
	v_fmac_f32_e32 v7, v30, v62
	s_waitcnt vmcnt(17)
	v_fmac_f32_e32 v7, v31, v63
	s_waitcnt vmcnt(16)
	v_fmac_f32_e32 v7, v24, v64
	s_waitcnt vmcnt(15)
	v_fmac_f32_e32 v7, v25, v36
	s_waitcnt vmcnt(14)
	v_fmac_f32_e32 v7, v26, v37
	s_waitcnt vmcnt(13)
	v_fmac_f32_e32 v7, v27, v47
	s_waitcnt vmcnt(7)
	v_fmac_f32_e32 v7, v12, v48
	v_add_co_u32_e32 v32, vcc, s3, v10
	v_fmac_f32_e32 v7, v13, v49
	s_nop 0
	v_addc_co_u32_e32 v33, vcc, 0, v11, vcc
	v_fmac_f32_e32 v7, v14, v50
	s_movk_i32 s3, 0x6000
	v_fmac_f32_e32 v7, v15, v65
	v_add_co_u32_e32 v10, vcc, s3, v10
	global_load_dword v34, v[42:43], off offset:1536
	global_load_dword v44, v[42:43], off offset:2048
	global_load_dword v45, v[42:43], off offset:2560
	global_load_dword v46, v[42:43], off offset:3072
	global_load_dword v35, v[32:33], off offset:512
	global_load_dword v36, v[32:33], off offset:1024
	global_load_dwordx4 v[12:15], v[8:9], off offset:176
	global_load_dwordx4 v[20:23], v[8:9], off offset:160
	s_waitcnt vmcnt(13)
	v_fmac_f32_e32 v7, v2, v38
	v_addc_co_u32_e32 v11, vcc, 0, v11, vcc
	global_load_dword v37, v[40:41], off offset:2560
	global_load_dword v38, v[40:41], off offset:3072
	global_load_dword v47, v[40:41], off offset:3584
	global_load_dword v48, v[10:11], off offset:-4096
	s_waitcnt vmcnt(16)
	v_fmac_f32_e32 v7, v3, v39
	s_waitcnt vmcnt(15)
	v_fmac_f32_e32 v7, v4, v51
	s_waitcnt vmcnt(14)
	v_fmac_f32_e32 v7, v5, v52
	global_load_dword v39, v[32:33], off offset:1536
	global_load_dword v40, v[32:33], off offset:2048
	global_load_dword v41, v[32:33], off offset:2560
	global_load_dword v49, v[32:33], off offset:3072
	global_load_dword v50, v[32:33], off offset:3584
	global_load_dwordx4 v[2:5], v[8:9], off offset:224
	global_load_dwordx4 v[24:27], v[8:9], off offset:208
	global_load_dwordx4 v[28:31], v[8:9], off offset:192
	global_load_dword v51, v[10:11], off
	global_load_dword v52, v[10:11], off offset:512
	global_load_dword v54, v[10:11], off offset:1024
	global_load_dword v55, v[10:11], off offset:1536
	global_load_dword v56, v[10:11], off offset:2048
	global_load_dword v57, v[10:11], off offset:2560
	global_load_dword v58, v[10:11], off offset:3072
	global_load_dword v32, v[10:11], off offset:3584
	global_load_dword v33, v[42:43], off
	global_load_dword v59, v[42:43], off offset:512
	global_load_dword v60, v[42:43], off offset:1024
	s_waitcnt vmcnt(31)
	v_fmac_f32_e32 v7, v16, v53
	global_load_dwordx4 v[8:11], v[8:9], off offset:240
	v_cmp_eq_u32_e32 vcc, 1, v1
	s_waitcnt vmcnt(23)
	v_fmac_f32_e32 v7, v17, v37
	s_waitcnt vmcnt(22)
	v_fmac_f32_e32 v7, v18, v38
	s_waitcnt vmcnt(21)
	v_fmac_f32_e32 v7, v19, v47
	s_waitcnt vmcnt(20)
	v_fmac_f32_e32 v7, v20, v48
	v_fmac_f32_e32 v7, v21, v35
	v_fmac_f32_e32 v7, v22, v36
	s_waitcnt vmcnt(19)
	v_fmac_f32_e32 v7, v23, v39
	s_waitcnt vmcnt(18)
	v_fmac_f32_e32 v7, v12, v40
	s_waitcnt vmcnt(17)
	v_fmac_f32_e32 v7, v13, v41
	s_waitcnt vmcnt(16)
	v_fmac_f32_e32 v7, v14, v49
	s_waitcnt vmcnt(15)
	v_fmac_f32_e32 v7, v15, v50
	s_waitcnt vmcnt(11)
	v_fmac_f32_e32 v7, v28, v51
	s_waitcnt vmcnt(10)
	v_fmac_f32_e32 v7, v29, v52
	s_waitcnt vmcnt(9)
	v_fmac_f32_e32 v7, v30, v54
	s_waitcnt vmcnt(8)
	v_fmac_f32_e32 v7, v31, v55
	s_waitcnt vmcnt(7)
	v_fmac_f32_e32 v7, v24, v56
	s_waitcnt vmcnt(6)
	v_fmac_f32_e32 v7, v25, v57
	s_waitcnt vmcnt(5)
	v_fmac_f32_e32 v7, v26, v58
	s_waitcnt vmcnt(4)
	v_fmac_f32_e32 v7, v27, v32
	s_waitcnt vmcnt(3)
	v_fmac_f32_e32 v7, v2, v33
	s_waitcnt vmcnt(2)
	v_fmac_f32_e32 v7, v3, v59
	s_waitcnt vmcnt(1)
	v_fmac_f32_e32 v7, v4, v60
	v_fmac_f32_e32 v7, v5, v34
	s_waitcnt vmcnt(0)
	v_fmac_f32_e32 v7, v8, v44
	v_fmac_f32_e32 v7, v9, v45
	v_fmac_f32_e32 v7, v10, v46
	v_fmac_f32_e32 v7, v11, v66
	s_and_saveexec_b64 s[6:7], vcc
	ds_write_b32 v6, v7
	s_or_b64 exec, exec, s[6:7]
	s_movk_i32 s3, 0x80
	v_cmp_gt_u32_e32 vcc, s3, v0
	s_waitcnt lgkmcnt(0)
	s_barrier
	s_and_saveexec_b64 s[6:7], vcc
	s_cbranch_execz .LBB0_10
	s_load_dwordx2 s[8:9], s[0:1], 0x50
	ds_read_b32 v4, v6
	v_or_b32_e32 v2, s4, v0
	v_mov_b32_e32 v3, 0
	s_waitcnt lgkmcnt(0)
	v_lshl_add_u64 v[2:3], v[2:3], 2, s[8:9]
	v_add_f32_e32 v4, v7, v4
	global_store_dword v[2:3], v4, off sc0 sc1

.LBB0_16:
	s_or_b64 exec, exec, s[4:5]
	v_add_u32_e32 v6, 0xfffffed4, v4
	v_cndmask_b32_e32 v5, 0, v5, vcc
	v_cndmask_b32_e32 v4, v6, v4, vcc
	v_and_b32_e32 v46, 0x7f, v0
	v_lshlrev_b64 v[4:5], 9, v[4:5]
	v_mov_b32_e32 v33, 0
	v_lshl_add_u64 v[4:5], v[8:9], 0, v[4:5]
	v_lshlrev_b32_e32 v32, 2, v46
	v_lshl_add_u64 v[34:35], v[4:5], 0, v[32:33]
	s_movk_i32 s3, 0x2000
	v_add_co_u32_e32 v36, vcc, s3, v34
	s_movk_i32 s4, 0x3000
	s_nop 0
	v_addc_co_u32_e32 v37, vcc, 0, v35, vcc
	global_load_dwordx4 v[4:7], v[2:3], off offset:80
	global_load_dword v38, v[36:37], off offset:2048
	global_load_dword v39, v[36:37], off offset:2560
	global_load_dword v40, v[36:37], off offset:3072
	global_load_dword v41, v[36:37], off offset:3584
	global_load_dwordx4 v[8:11], v[2:3], off offset:64
	global_load_dword v42, v[36:37], off offset:1024
	global_load_dword v43, v[36:37], off offset:1536
	global_load_dwordx4 v[12:15], v[2:3], off offset:48
	global_load_dwordx4 v[16:19], v[2:3], off offset:32
	global_load_dwordx4 v[20:23], v[2:3], off offset:16
	global_load_dwordx4 v[24:27], v[2:3], off
	global_load_dwordx2 v[44:45], v[2:3], off offset:112
	global_load_dwordx4 v[28:31], v[2:3], off offset:96
	v_add_co_u32_e32 v2, vcc, s4, v34
	v_lshl_or_b32 v32, v1, 7, v46
	s_nop 0
	v_addc_co_u32_e32 v3, vcc, 0, v35, vcc
	global_load_dword v46, v[2:3], off
	global_load_dword v1, v[36:37], off offset:-4096
	global_load_dword v52, v[36:37], off
	global_load_dword v53, v[36:37], off offset:512
	global_load_dword v47, v[2:3], off offset:512
	global_load_dword v48, v[2:3], off offset:1024
	global_load_dword v49, v[2:3], off offset:1536
	global_load_dword v50, v[2:3], off offset:2048
	global_load_dword v51, v[2:3], off offset:2560
	global_load_dword v54, v[34:35], off
	global_load_dword v55, v[34:35], off offset:512
	global_load_dword v56, v[34:35], off offset:1024
	global_load_dword v57, v[34:35], off offset:1536
	global_load_dword v58, v[34:35], off offset:2048
	global_load_dword v59, v[34:35], off offset:2560
	global_load_dword v36, v[34:35], off offset:3072
	global_load_dword v37, v[34:35], off offset:3584
	s_movk_i32 s3, 0x1000
	v_add_co_u32_e32 v2, vcc, s3, v34
	s_nop 1
	v_addc_co_u32_e32 v3, vcc, 0, v35, vcc
	s_waitcnt vmcnt(28)
	v_pk_mul_f32 v[4:5], v[4:5], v[38:39]
	s_waitcnt vmcnt(26)
	v_pk_mul_f32 v[6:7], v[6:7], v[40:41]
	global_load_dword v34, v[2:3], off offset:512
	global_load_dword v35, v[2:3], off offset:1024
	global_load_dword v38, v[2:3], off offset:1536
	global_load_dword v39, v[2:3], off offset:2048
	global_load_dword v40, v[2:3], off offset:2560
	global_load_dword v41, v[2:3], off offset:3072
	global_load_dword v60, v[2:3], off offset:3584
	s_waitcnt vmcnt(30)
	v_pk_mul_f32 v[2:3], v[10:11], v[42:43]
	s_waitcnt vmcnt(14)
	v_fma_f32 v54, v24, v54, 0
	s_waitcnt vmcnt(13)
	v_fmac_f32_e32 v54, v25, v55
	s_waitcnt vmcnt(12)
	v_fmac_f32_e32 v54, v26, v56
	s_waitcnt vmcnt(11)
	v_fmac_f32_e32 v54, v27, v57
	s_waitcnt vmcnt(10)
	v_fmac_f32_e32 v54, v20, v58
	s_waitcnt vmcnt(9)
	v_fmac_f32_e32 v54, v21, v59
	s_waitcnt vmcnt(8)
	v_fmac_f32_e32 v54, v22, v36
	s_waitcnt vmcnt(7)
	v_fmac_f32_e32 v54, v23, v37
	v_fmac_f32_e32 v54, v16, v1
	v_pk_mul_f32 v[10:11], v[28:29], v[46:47]
	v_pk_mul_f32 v[24:25], v[30:31], v[48:49]
	v_pk_mul_f32 v[28:29], v[44:45], v[50:51]
	s_waitcnt vmcnt(6)
	v_fmac_f32_e32 v54, v17, v34
	s_waitcnt vmcnt(5)
	v_fmac_f32_e32 v54, v18, v35
	s_waitcnt vmcnt(4)
	v_fmac_f32_e32 v54, v19, v38
	s_waitcnt vmcnt(3)
	v_fmac_f32_e32 v54, v12, v39
	s_waitcnt vmcnt(2)
	v_fmac_f32_e32 v54, v13, v40
	s_waitcnt vmcnt(1)
	v_fmac_f32_e32 v54, v14, v41
	s_waitcnt vmcnt(0)
	v_fmac_f32_e32 v54, v15, v60
	v_fmac_f32_e32 v54, v8, v52
	v_fmac_f32_e32 v54, v9, v53
	v_add_f32_e32 v1, v54, v2
	v_add_f32_e32 v1, v1, v3
	v_add_f32_e32 v1, v1, v4
	v_add_f32_e32 v1, v1, v5
	v_add_f32_e32 v1, v1, v6
	v_add_f32_e32 v1, v1, v7
	v_add_f32_e32 v1, v1, v10
	v_add_f32_e32 v1, v1, v11
	v_add_f32_e32 v1, v1, v24
	v_add_f32_e32 v1, v1, v25
	v_add_f32_e32 v1, v1, v28
	v_add_f32_e32 v1, v1, v29
	v_lshl_add_u64 v[2:3], v[32:33], 2, s[6:7]
	global_store_dword v[2:3], v1, off sc0 sc1
	s_cbranch_execnz .LBB0_3
	s_branch .LBB0_18

.LBB0_18:
	s_load_dwordx4 s[4:7], s[0:1], 0x0
	v_lshl_add_u32 v4, s2, 8, v0
	v_lshrrev_b32_e32 v1, 1, v0
	v_and_b32_e32 v2, 31, v0
	s_movk_i32 s2, 0x60
	v_lshrrev_b32_e32 v0, 2, v0
	v_and_or_b32 v1, v1, s2, v2
	v_ashrrev_i32_e32 v2, 5, v4
	v_and_b32_e32 v0, 8, v0
	v_and_or_b32 v0, v2, -16, v0
	v_and_b32_e32 v2, 0x100, v4
	s_waitcnt lgkmcnt(0)
	v_mov_b32_e32 v3, s7
	v_mov_b32_e32 v5, s5
	v_cmp_eq_u32_e32 vcc, 0, v2
	v_mov_b32_e32 v2, s6
	v_lshlrev_b32_e32 v6, 2, v1
	v_cndmask_b32_e32 v3, v3, v5, vcc
	v_mov_b32_e32 v5, s4
	v_cndmask_b32_e32 v2, v2, v5, vcc
	v_mov_b32_e32 v7, 0
	v_ashrrev_i32_e32 v1, 31, v0
	v_or_b32_e32 v10, 2, v0
	v_lshl_add_u64 v[2:3], v[2:3], 0, v[6:7]
	v_lshlrev_b64 v[6:7], 9, v[0:1]
	v_or_b32_e32 v8, 1, v0
	v_ashrrev_i32_e32 v11, 31, v10
	v_or_b32_e32 v12, 3, v0
	v_or_b32_e32 v14, 4, v0
	v_or_b32_e32 v16, 5, v0
	v_or_b32_e32 v18, 6, v0
	v_or_b32_e32 v0, 7, v0
	v_ashrrev_i32_e32 v9, 31, v8
	v_lshlrev_b64 v[10:11], 9, v[10:11]
	v_ashrrev_i32_e32 v13, 31, v12
	v_ashrrev_i32_e32 v15, 31, v14
	v_ashrrev_i32_e32 v17, 31, v16
	v_ashrrev_i32_e32 v19, 31, v18
	v_ashrrev_i32_e32 v1, 31, v0
	v_lshlrev_b64 v[8:9], 9, v[8:9]
	v_lshl_add_u64 v[10:11], v[2:3], 0, v[10:11]
	v_lshlrev_b64 v[12:13], 9, v[12:13]
	v_lshlrev_b64 v[14:15], 9, v[14:15]
	v_lshlrev_b64 v[16:17], 9, v[16:17]
	v_lshlrev_b64 v[18:19], 9, v[18:19]
	v_lshlrev_b64 v[0:1], 9, v[0:1]
	v_lshl_add_u64 v[6:7], v[2:3], 0, v[6:7]
	v_lshl_add_u64 v[8:9], v[2:3], 0, v[8:9]
	v_lshl_add_u64 v[12:13], v[2:3], 0, v[12:13]
	v_lshl_add_u64 v[14:15], v[2:3], 0, v[14:15]
	v_lshl_add_u64 v[16:17], v[2:3], 0, v[16:17]
	v_lshl_add_u64 v[18:19], v[2:3], 0, v[18:19]
	v_lshl_add_u64 v[0:1], v[2:3], 0, v[0:1]
	global_load_dword v20, v[10:11], off
	global_load_dword v21, v[12:13], off
	global_load_dword v2, v[14:15], off
	global_load_dword v3, v[18:19], off
	global_load_dword v22, v[0:1], off
	global_load_dword v23, v[16:17], off
	global_load_dword v24, v[6:7], off
	global_load_dword v25, v[8:9], off
	s_load_dwordx2 s[0:1], s[0:1], 0x40
	v_ashrrev_i32_e32 v5, 31, v4
	s_waitcnt lgkmcnt(0)
	v_lshl_add_u64 v[4:5], v[4:5], 4, s[0:1]
	s_waitcnt vmcnt(6)
	v_cvt_pk_f16_f32 v1, v20, v21
	s_waitcnt vmcnt(3)
	v_cvt_pk_f16_f32 v3, v3, v22
	s_waitcnt vmcnt(2)
	v_cvt_pk_f16_f32 v2, v2, v23
	s_waitcnt vmcnt(0)
	v_cvt_pk_f16_f32 v0, v24, v25
	global_store_dwordx4 v[4:5], v[0:3], off sc0 sc1
	s_endpgm
